# select: group-skip late passes, bank-interleaved pass-1 histogram copies
# speedup vs baseline: 1.0335x; 1.0220x over previous
.LBB0_580:
	v_mov_b32_e32 v2, v0
	s_nop 0
	v_readfirstlane_b32 s0, v2
	s_bfe_u32 s14, s0, 0x30006
	s_lshl_b32 s0, s4, 4
	s_lshl_b32 s1, s14, 1
	s_or_b32 s92, s1, s0
	s_or_b32 s22, s92, 1
	s_add_i32 s31, s92, 2
	v_and_b32_e32 v146, 63, v2
	s_cmpk_gt_u32 s92, 0xfe
	s_mov_b64 s[0:1], -1
	s_cbranch_scc0 .LBB0_602
	s_lshl_b32 s2, s14, 14
	v_lshl_add_u32 v7, v146, 2, s2
	s_lshr_b32 s3, s92, 6
	s_mul_i32 s5, s14, 0xa00
	s_add_i32 s5, s5, 0x20000
	s_add_i32 s6, s5, 0x500
	v_mov_b32_e32 v199, 1
	v_mov_b32_e32 v248, 0
	v_mov_b32_e32 v249, 0
	v_mov_b32_e32 v250, 0
	v_mov_b32_e32 v251, 0
	v_mov_b32_e32 v2, 0
	v_mov_b32_e32 v3, 0
	v_mov_b32_e32 v4, 0
	v_mov_b32_e32 v5, 0
	v_lshl_add_u32 v195, v146, 4, s5
	v_add_u32_e32 v247, 0x100, v146
	v_lshl_add_u32 v197, v146, 4, s2
	v_and_b32_e32 v188, 7, v146
	v_lshl_add_u32 v188, v188, 2, s2
	v_lshl_add_u32 v178, v146, 7, s2
	v_add_u32_e32 v189, 0x2000, v188
	s_mov_b32 s7, 0
	s_mov_b32 s8, 0
	s_movk_i32 s9, 0x100
	s_movk_i32 s10, 0x100
	s_mov_b32 s12, 0
	s_mov_b32 s13, 0
	ds_read2st64_b32 v[200:201], v7 offset0:0 offset1:1
	ds_read2st64_b32 v[202:203], v7 offset0:2 offset1:3
	ds_read2st64_b32 v[148:149], v7 offset0:32 offset1:33
	ds_read2st64_b32 v[150:151], v7 offset0:34 offset1:35
	s_waitcnt lgkmcnt(3)
	v_ashrrev_i32_e32 v9, 31, v200
	v_bitop3_b32 v200, v9, v200, s30 bitop3:0x36
	v_ashrrev_i32_e32 v10, 31, v201
	v_bitop3_b32 v201, v10, v201, s30 bitop3:0x36
	s_waitcnt lgkmcnt(2)
	v_ashrrev_i32_e32 v11, 31, v202
	v_bitop3_b32 v202, v11, v202, s30 bitop3:0x36
	v_ashrrev_i32_e32 v12, 31, v203
	v_bitop3_b32 v203, v12, v203, s30 bitop3:0x36
	s_waitcnt lgkmcnt(1)
	v_ashrrev_i32_e32 v9, 31, v148
	v_bitop3_b32 v148, v9, v148, s30 bitop3:0x36
	v_ashrrev_i32_e32 v10, 31, v149
	v_bitop3_b32 v149, v10, v149, s30 bitop3:0x36
	s_waitcnt lgkmcnt(0)
	v_ashrrev_i32_e32 v11, 31, v150
	v_bitop3_b32 v150, v11, v150, s30 bitop3:0x36
	v_ashrrev_i32_e32 v12, 31, v151
	v_bitop3_b32 v151, v12, v151, s30 bitop3:0x36
	ds_read2st64_b32 v[204:205], v7 offset0:4 offset1:5
	ds_read2st64_b32 v[206:207], v7 offset0:6 offset1:7
	ds_read2st64_b32 v[152:153], v7 offset0:36 offset1:37
	ds_read2st64_b32 v[154:155], v7 offset0:38 offset1:39
	s_waitcnt lgkmcnt(3)
	v_ashrrev_i32_e32 v9, 31, v204
	v_bitop3_b32 v204, v9, v204, s30 bitop3:0x36
	v_ashrrev_i32_e32 v10, 31, v205
	v_bitop3_b32 v205, v10, v205, s30 bitop3:0x36
	s_waitcnt lgkmcnt(2)
	v_ashrrev_i32_e32 v11, 31, v206
	v_bitop3_b32 v206, v11, v206, s30 bitop3:0x36
	v_ashrrev_i32_e32 v12, 31, v207
	v_bitop3_b32 v207, v12, v207, s30 bitop3:0x36
	s_waitcnt lgkmcnt(1)
	v_ashrrev_i32_e32 v9, 31, v152
	v_bitop3_b32 v152, v9, v152, s30 bitop3:0x36
	v_ashrrev_i32_e32 v10, 31, v153
	v_bitop3_b32 v153, v10, v153, s30 bitop3:0x36
	s_waitcnt lgkmcnt(0)
	v_ashrrev_i32_e32 v11, 31, v154
	v_bitop3_b32 v154, v11, v154, s30 bitop3:0x36
	v_ashrrev_i32_e32 v12, 31, v155
	v_bitop3_b32 v155, v12, v155, s30 bitop3:0x36
	s_cmp_lt_u32 s3, 8
	s_cbranch_scc1 .Lsel_fix1_3
	ds_read2st64_b32 v[208:209], v7 offset0:8 offset1:9
	ds_read2st64_b32 v[210:211], v7 offset0:10 offset1:11
	ds_read2st64_b32 v[156:157], v7 offset0:40 offset1:41
	ds_read2st64_b32 v[158:159], v7 offset0:42 offset1:43
	s_waitcnt lgkmcnt(3)
	v_ashrrev_i32_e32 v9, 31, v208
	v_bitop3_b32 v208, v9, v208, s30 bitop3:0x36
	v_ashrrev_i32_e32 v10, 31, v209
	v_bitop3_b32 v209, v10, v209, s30 bitop3:0x36
	s_waitcnt lgkmcnt(2)
	v_ashrrev_i32_e32 v11, 31, v210
	v_bitop3_b32 v210, v11, v210, s30 bitop3:0x36
	v_ashrrev_i32_e32 v12, 31, v211
	v_bitop3_b32 v211, v12, v211, s30 bitop3:0x36
	s_waitcnt lgkmcnt(1)
	v_ashrrev_i32_e32 v9, 31, v156
	v_bitop3_b32 v156, v9, v156, s30 bitop3:0x36
	v_ashrrev_i32_e32 v10, 31, v157
	v_bitop3_b32 v157, v10, v157, s30 bitop3:0x36
	s_waitcnt lgkmcnt(0)
	v_ashrrev_i32_e32 v11, 31, v158
	v_bitop3_b32 v158, v11, v158, s30 bitop3:0x36
	v_ashrrev_i32_e32 v12, 31, v159
	v_bitop3_b32 v159, v12, v159, s30 bitop3:0x36
	s_cmp_lt_u32 s3, 12
	s_cbranch_scc1 .Lsel_fix2_4
	ds_read2st64_b32 v[212:213], v7 offset0:12 offset1:13
	ds_read2st64_b32 v[214:215], v7 offset0:14 offset1:15
	ds_read2st64_b32 v[160:161], v7 offset0:44 offset1:45
	ds_read2st64_b32 v[162:163], v7 offset0:46 offset1:47
	s_waitcnt lgkmcnt(3)
	v_ashrrev_i32_e32 v9, 31, v212
	v_bitop3_b32 v212, v9, v212, s30 bitop3:0x36
	v_ashrrev_i32_e32 v10, 31, v213
	v_bitop3_b32 v213, v10, v213, s30 bitop3:0x36
	s_waitcnt lgkmcnt(2)
	v_ashrrev_i32_e32 v11, 31, v214
	v_bitop3_b32 v214, v11, v214, s30 bitop3:0x36
	v_ashrrev_i32_e32 v12, 31, v215
	v_bitop3_b32 v215, v12, v215, s30 bitop3:0x36
	s_waitcnt lgkmcnt(1)
	v_ashrrev_i32_e32 v9, 31, v160
	v_bitop3_b32 v160, v9, v160, s30 bitop3:0x36
	v_ashrrev_i32_e32 v10, 31, v161
	v_bitop3_b32 v161, v10, v161, s30 bitop3:0x36
	s_waitcnt lgkmcnt(0)
	v_ashrrev_i32_e32 v11, 31, v162
	v_bitop3_b32 v162, v11, v162, s30 bitop3:0x36
	v_ashrrev_i32_e32 v12, 31, v163
	v_bitop3_b32 v163, v12, v163, s30 bitop3:0x36
	s_cmp_lt_u32 s3, 16
	s_cbranch_scc1 .Lsel_fix3_5
	ds_read2st64_b32 v[216:217], v7 offset0:16 offset1:17
	ds_read2st64_b32 v[218:219], v7 offset0:18 offset1:19
	ds_read2st64_b32 v[164:165], v7 offset0:48 offset1:49
	ds_read2st64_b32 v[166:167], v7 offset0:50 offset1:51
	s_waitcnt lgkmcnt(3)
	v_ashrrev_i32_e32 v9, 31, v216
	v_bitop3_b32 v216, v9, v216, s30 bitop3:0x36
	v_ashrrev_i32_e32 v10, 31, v217
	v_bitop3_b32 v217, v10, v217, s30 bitop3:0x36
	s_waitcnt lgkmcnt(2)
	v_ashrrev_i32_e32 v11, 31, v218
	v_bitop3_b32 v218, v11, v218, s30 bitop3:0x36
	v_ashrrev_i32_e32 v12, 31, v219
	v_bitop3_b32 v219, v12, v219, s30 bitop3:0x36
	s_waitcnt lgkmcnt(1)
	v_ashrrev_i32_e32 v9, 31, v164
	v_bitop3_b32 v164, v9, v164, s30 bitop3:0x36
	v_ashrrev_i32_e32 v10, 31, v165
	v_bitop3_b32 v165, v10, v165, s30 bitop3:0x36
	s_waitcnt lgkmcnt(0)
	v_ashrrev_i32_e32 v11, 31, v166
	v_bitop3_b32 v166, v11, v166, s30 bitop3:0x36
	v_ashrrev_i32_e32 v12, 31, v167
	v_bitop3_b32 v167, v12, v167, s30 bitop3:0x36
	s_cmp_lt_u32 s3, 20
	s_cbranch_scc1 .Lsel_fix4_6
	ds_read2st64_b32 v[220:221], v7 offset0:20 offset1:21
	ds_read2st64_b32 v[222:223], v7 offset0:22 offset1:23
	ds_read2st64_b32 v[168:169], v7 offset0:52 offset1:53
	ds_read2st64_b32 v[170:171], v7 offset0:54 offset1:55
	s_waitcnt lgkmcnt(3)
	v_ashrrev_i32_e32 v9, 31, v220
	v_bitop3_b32 v220, v9, v220, s30 bitop3:0x36
	v_ashrrev_i32_e32 v10, 31, v221
	v_bitop3_b32 v221, v10, v221, s30 bitop3:0x36
	s_waitcnt lgkmcnt(2)
	v_ashrrev_i32_e32 v11, 31, v222
	v_bitop3_b32 v222, v11, v222, s30 bitop3:0x36
	v_ashrrev_i32_e32 v12, 31, v223
	v_bitop3_b32 v223, v12, v223, s30 bitop3:0x36
	s_waitcnt lgkmcnt(1)
	v_ashrrev_i32_e32 v9, 31, v168
	v_bitop3_b32 v168, v9, v168, s30 bitop3:0x36
	v_ashrrev_i32_e32 v10, 31, v169
	v_bitop3_b32 v169, v10, v169, s30 bitop3:0x36
	s_waitcnt lgkmcnt(0)
	v_ashrrev_i32_e32 v11, 31, v170
	v_bitop3_b32 v170, v11, v170, s30 bitop3:0x36
	v_ashrrev_i32_e32 v12, 31, v171
	v_bitop3_b32 v171, v12, v171, s30 bitop3:0x36
	s_cmp_lt_u32 s3, 24
	s_cbranch_scc1 .Lsel_fix5_7
	ds_read2st64_b32 v[224:225], v7 offset0:24 offset1:25
	ds_read2st64_b32 v[226:227], v7 offset0:26 offset1:27
	ds_read2st64_b32 v[172:173], v7 offset0:56 offset1:57
	ds_read2st64_b32 v[174:175], v7 offset0:58 offset1:59
	s_waitcnt lgkmcnt(3)
	v_ashrrev_i32_e32 v9, 31, v224
	v_bitop3_b32 v224, v9, v224, s30 bitop3:0x36
	v_ashrrev_i32_e32 v10, 31, v225
	v_bitop3_b32 v225, v10, v225, s30 bitop3:0x36
	s_waitcnt lgkmcnt(2)
	v_ashrrev_i32_e32 v11, 31, v226
	v_bitop3_b32 v226, v11, v226, s30 bitop3:0x36
	v_ashrrev_i32_e32 v12, 31, v227
	v_bitop3_b32 v227, v12, v227, s30 bitop3:0x36
	s_waitcnt lgkmcnt(1)
	v_ashrrev_i32_e32 v9, 31, v172
	v_bitop3_b32 v172, v9, v172, s30 bitop3:0x36
	v_ashrrev_i32_e32 v10, 31, v173
	v_bitop3_b32 v173, v10, v173, s30 bitop3:0x36
	s_waitcnt lgkmcnt(0)
	v_ashrrev_i32_e32 v11, 31, v174
	v_bitop3_b32 v174, v11, v174, s30 bitop3:0x36
	v_ashrrev_i32_e32 v12, 31, v175
	v_bitop3_b32 v175, v12, v175, s30 bitop3:0x36
	s_cmp_lt_u32 s3, 28
	s_cbranch_scc1 .Lsel_fix6_8
	ds_read2st64_b32 v[228:229], v7 offset0:28 offset1:29
	ds_read2st64_b32 v[230:231], v7 offset0:30 offset1:31
	ds_read2st64_b32 v[176:177], v7 offset0:60 offset1:61
	ds_read2st64_b32 v[186:187], v7 offset0:62 offset1:63
	s_waitcnt lgkmcnt(3)
	v_ashrrev_i32_e32 v9, 31, v228
	v_bitop3_b32 v228, v9, v228, s30 bitop3:0x36
	v_ashrrev_i32_e32 v10, 31, v229
	v_bitop3_b32 v229, v10, v229, s30 bitop3:0x36
	s_waitcnt lgkmcnt(2)
	v_ashrrev_i32_e32 v11, 31, v230
	v_bitop3_b32 v230, v11, v230, s30 bitop3:0x36
	v_ashrrev_i32_e32 v12, 31, v231
	v_bitop3_b32 v231, v12, v231, s30 bitop3:0x36
	s_waitcnt lgkmcnt(1)
	v_ashrrev_i32_e32 v9, 31, v176
	v_bitop3_b32 v176, v9, v176, s30 bitop3:0x36
	v_ashrrev_i32_e32 v10, 31, v177
	v_bitop3_b32 v177, v10, v177, s30 bitop3:0x36
	s_waitcnt lgkmcnt(0)
	v_ashrrev_i32_e32 v11, 31, v186
	v_bitop3_b32 v186, v11, v186, s30 bitop3:0x36
	v_ashrrev_i32_e32 v12, 31, v187
	v_bitop3_b32 v187, v12, v187, s30 bitop3:0x36
	s_branch .Lsel_fix7_9

.Lsel_load_done_1:
	ds_write_b128 v197, v[248:251] offset:0
	ds_write_b128 v197, v[248:251] offset:1024
	ds_write_b128 v197, v[248:251] offset:2048
	ds_write_b128 v197, v[248:251] offset:3072
	ds_write_b128 v197, v[248:251] offset:4096
	ds_write_b128 v197, v[248:251] offset:5120
	ds_write_b128 v197, v[248:251] offset:6144
	ds_write_b128 v197, v[248:251] offset:7168
	ds_write_b128 v197, v[248:251] offset:8192
	ds_write_b128 v197, v[248:251] offset:9216
	ds_write_b128 v197, v[248:251] offset:10240
	ds_write_b128 v197, v[248:251] offset:11264
	ds_write_b128 v197, v[248:251] offset:12288
	ds_write_b128 v197, v[248:251] offset:13312
	ds_write_b128 v197, v[248:251] offset:14336
	ds_write_b128 v197, v[248:251] offset:15360
	v_lshrrev_b32_e32 v9, 24, v200
	v_lshl_add_u32 v9, v9, 5, v188
	ds_add_u32 v9, v199
	v_lshrrev_b32_e32 v10, 24, v201
	v_lshl_add_u32 v10, v10, 5, v188
	ds_add_u32 v10, v199
	v_lshrrev_b32_e32 v11, 24, v202
	v_lshl_add_u32 v11, v11, 5, v188
	ds_add_u32 v11, v199
	v_lshrrev_b32_e32 v12, 24, v203
	v_lshl_add_u32 v12, v12, 5, v188
	ds_add_u32 v12, v199
	v_lshrrev_b32_e32 v13, 24, v148
	v_lshl_add_u32 v13, v13, 5, v189
	ds_add_u32 v13, v199
	v_lshrrev_b32_e32 v180, 24, v149
	v_lshl_add_u32 v180, v180, 5, v189
	ds_add_u32 v180, v199
	v_lshrrev_b32_e32 v182, 24, v150
	v_lshl_add_u32 v182, v182, 5, v189
	ds_add_u32 v182, v199
	v_lshrrev_b32_e32 v183, 24, v151
	v_lshl_add_u32 v183, v183, 5, v189
	ds_add_u32 v183, v199
	v_lshrrev_b32_e32 v9, 24, v204
	v_lshl_add_u32 v9, v9, 5, v188
	ds_add_u32 v9, v199
	v_lshrrev_b32_e32 v10, 24, v205
	v_lshl_add_u32 v10, v10, 5, v188
	ds_add_u32 v10, v199
	v_lshrrev_b32_e32 v11, 24, v206
	v_lshl_add_u32 v11, v11, 5, v188
	ds_add_u32 v11, v199
	v_lshrrev_b32_e32 v12, 24, v207
	v_lshl_add_u32 v12, v12, 5, v188
	ds_add_u32 v12, v199
	v_lshrrev_b32_e32 v13, 24, v152
	v_lshl_add_u32 v13, v13, 5, v189
	ds_add_u32 v13, v199
	v_lshrrev_b32_e32 v180, 24, v153
	v_lshl_add_u32 v180, v180, 5, v189
	ds_add_u32 v180, v199
	v_lshrrev_b32_e32 v182, 24, v154
	v_lshl_add_u32 v182, v182, 5, v189
	ds_add_u32 v182, v199
	v_lshrrev_b32_e32 v183, 24, v155
	v_lshl_add_u32 v183, v183, 5, v189
	ds_add_u32 v183, v199
	s_cmp_lt_u32 s3, 8
	s_cbranch_scc1 .Lsel_p1_done_10
	v_lshrrev_b32_e32 v9, 24, v208
	v_lshl_add_u32 v9, v9, 5, v188
	ds_add_u32 v9, v199
	v_lshrrev_b32_e32 v10, 24, v209
	v_lshl_add_u32 v10, v10, 5, v188
	ds_add_u32 v10, v199
	v_lshrrev_b32_e32 v11, 24, v210
	v_lshl_add_u32 v11, v11, 5, v188
	ds_add_u32 v11, v199
	v_lshrrev_b32_e32 v12, 24, v211
	v_lshl_add_u32 v12, v12, 5, v188
	ds_add_u32 v12, v199
	v_lshrrev_b32_e32 v13, 24, v156
	v_lshl_add_u32 v13, v13, 5, v189
	ds_add_u32 v13, v199
	v_lshrrev_b32_e32 v180, 24, v157
	v_lshl_add_u32 v180, v180, 5, v189
	ds_add_u32 v180, v199
	v_lshrrev_b32_e32 v182, 24, v158
	v_lshl_add_u32 v182, v182, 5, v189
	ds_add_u32 v182, v199
	v_lshrrev_b32_e32 v183, 24, v159
	v_lshl_add_u32 v183, v183, 5, v189
	ds_add_u32 v183, v199
	s_cmp_lt_u32 s3, 12
	s_cbranch_scc1 .Lsel_p1_done_10
	v_lshrrev_b32_e32 v9, 24, v212
	v_lshl_add_u32 v9, v9, 5, v188
	ds_add_u32 v9, v199
	v_lshrrev_b32_e32 v10, 24, v213
	v_lshl_add_u32 v10, v10, 5, v188
	ds_add_u32 v10, v199
	v_lshrrev_b32_e32 v11, 24, v214
	v_lshl_add_u32 v11, v11, 5, v188
	ds_add_u32 v11, v199
	v_lshrrev_b32_e32 v12, 24, v215
	v_lshl_add_u32 v12, v12, 5, v188
	ds_add_u32 v12, v199
	v_lshrrev_b32_e32 v13, 24, v160
	v_lshl_add_u32 v13, v13, 5, v189
	ds_add_u32 v13, v199
	v_lshrrev_b32_e32 v180, 24, v161
	v_lshl_add_u32 v180, v180, 5, v189
	ds_add_u32 v180, v199
	v_lshrrev_b32_e32 v182, 24, v162
	v_lshl_add_u32 v182, v182, 5, v189
	ds_add_u32 v182, v199
	v_lshrrev_b32_e32 v183, 24, v163
	v_lshl_add_u32 v183, v183, 5, v189
	ds_add_u32 v183, v199
	s_cmp_lt_u32 s3, 16
	s_cbranch_scc1 .Lsel_p1_done_10
	v_lshrrev_b32_e32 v9, 24, v216
	v_lshl_add_u32 v9, v9, 5, v188
	ds_add_u32 v9, v199
	v_lshrrev_b32_e32 v10, 24, v217
	v_lshl_add_u32 v10, v10, 5, v188
	ds_add_u32 v10, v199
	v_lshrrev_b32_e32 v11, 24, v218
	v_lshl_add_u32 v11, v11, 5, v188
	ds_add_u32 v11, v199
	v_lshrrev_b32_e32 v12, 24, v219
	v_lshl_add_u32 v12, v12, 5, v188
	ds_add_u32 v12, v199
	v_lshrrev_b32_e32 v13, 24, v164
	v_lshl_add_u32 v13, v13, 5, v189
	ds_add_u32 v13, v199
	v_lshrrev_b32_e32 v180, 24, v165
	v_lshl_add_u32 v180, v180, 5, v189
	ds_add_u32 v180, v199
	v_lshrrev_b32_e32 v182, 24, v166
	v_lshl_add_u32 v182, v182, 5, v189
	ds_add_u32 v182, v199
	v_lshrrev_b32_e32 v183, 24, v167
	v_lshl_add_u32 v183, v183, 5, v189
	ds_add_u32 v183, v199
	s_cmp_lt_u32 s3, 20
	s_cbranch_scc1 .Lsel_p1_done_10
	v_lshrrev_b32_e32 v9, 24, v220
	v_lshl_add_u32 v9, v9, 5, v188
	ds_add_u32 v9, v199
	v_lshrrev_b32_e32 v10, 24, v221
	v_lshl_add_u32 v10, v10, 5, v188
	ds_add_u32 v10, v199
	v_lshrrev_b32_e32 v11, 24, v222
	v_lshl_add_u32 v11, v11, 5, v188
	ds_add_u32 v11, v199
	v_lshrrev_b32_e32 v12, 24, v223
	v_lshl_add_u32 v12, v12, 5, v188
	ds_add_u32 v12, v199
	v_lshrrev_b32_e32 v13, 24, v168
	v_lshl_add_u32 v13, v13, 5, v189
	ds_add_u32 v13, v199
	v_lshrrev_b32_e32 v180, 24, v169
	v_lshl_add_u32 v180, v180, 5, v189
	ds_add_u32 v180, v199
	v_lshrrev_b32_e32 v182, 24, v170
	v_lshl_add_u32 v182, v182, 5, v189
	ds_add_u32 v182, v199
	v_lshrrev_b32_e32 v183, 24, v171
	v_lshl_add_u32 v183, v183, 5, v189
	ds_add_u32 v183, v199
	s_cmp_lt_u32 s3, 24
	s_cbranch_scc1 .Lsel_p1_done_10
	v_lshrrev_b32_e32 v9, 24, v224
	v_lshl_add_u32 v9, v9, 5, v188
	ds_add_u32 v9, v199
	v_lshrrev_b32_e32 v10, 24, v225
	v_lshl_add_u32 v10, v10, 5, v188
	ds_add_u32 v10, v199
	v_lshrrev_b32_e32 v11, 24, v226
	v_lshl_add_u32 v11, v11, 5, v188
	ds_add_u32 v11, v199
	v_lshrrev_b32_e32 v12, 24, v227
	v_lshl_add_u32 v12, v12, 5, v188
	ds_add_u32 v12, v199
	v_lshrrev_b32_e32 v13, 24, v172
	v_lshl_add_u32 v13, v13, 5, v189
	ds_add_u32 v13, v199
	v_lshrrev_b32_e32 v180, 24, v173
	v_lshl_add_u32 v180, v180, 5, v189
	ds_add_u32 v180, v199
	v_lshrrev_b32_e32 v182, 24, v174
	v_lshl_add_u32 v182, v182, 5, v189
	ds_add_u32 v182, v199
	v_lshrrev_b32_e32 v183, 24, v175
	v_lshl_add_u32 v183, v183, 5, v189
	ds_add_u32 v183, v199
	s_cmp_lt_u32 s3, 28
	s_cbranch_scc1 .Lsel_p1_done_10
	v_lshrrev_b32_e32 v9, 24, v228
	v_lshl_add_u32 v9, v9, 5, v188
	ds_add_u32 v9, v199
	v_lshrrev_b32_e32 v10, 24, v229
	v_lshl_add_u32 v10, v10, 5, v188
	ds_add_u32 v10, v199
	v_lshrrev_b32_e32 v11, 24, v230
	v_lshl_add_u32 v11, v11, 5, v188
	ds_add_u32 v11, v199
	v_lshrrev_b32_e32 v12, 24, v231
	v_lshl_add_u32 v12, v12, 5, v188
	ds_add_u32 v12, v199
	v_lshrrev_b32_e32 v13, 24, v176
	v_lshl_add_u32 v13, v13, 5, v189
	ds_add_u32 v13, v199
	v_lshrrev_b32_e32 v180, 24, v177
	v_lshl_add_u32 v180, v180, 5, v189
	ds_add_u32 v180, v199
	v_lshrrev_b32_e32 v182, 24, v186
	v_lshl_add_u32 v182, v182, 5, v189
	ds_add_u32 v182, v199
	v_lshrrev_b32_e32 v183, 24, v187
	v_lshl_add_u32 v183, v183, 5, v189
	ds_add_u32 v183, v199
.Lsel_p1_done_10:
	s_movk_i32 s11, 24
	s_waitcnt lgkmcnt(0)
	ds_read_b128 v[16:19], v178 offset:0
	ds_read_b128 v[20:23], v178 offset:16
	ds_read_b128 v[24:27], v178 offset:32
	ds_read_b128 v[28:31], v178 offset:48
	ds_read_b128 v[190:193], v178 offset:64
	ds_read_b128 v[10:13], v178 offset:80
	ds_read_b128 v[180:183], v178 offset:96
	ds_read_b128 v[6:9], v178 offset:112
	s_waitcnt lgkmcnt(0)
	v_add3_u32 v232, v16, v17, v18
	v_add3_u32 v19, v19, v20, v21
	v_add3_u32 v232, v232, v22, v23
	v_add_u32_e32 v232, v232, v19
	v_add3_u32 v233, v24, v25, v26
	v_add3_u32 v27, v27, v28, v29
	v_add3_u32 v233, v233, v30, v31
	v_add_u32_e32 v233, v233, v27
	v_add3_u32 v234, v190, v191, v192
	v_add3_u32 v193, v193, v10, v11
	v_add3_u32 v234, v234, v12, v13
	v_add_u32_e32 v234, v234, v193
	v_add3_u32 v235, v180, v181, v182
	v_add3_u32 v183, v183, v6, v7
	v_add3_u32 v235, v235, v8, v9
	v_add_u32_e32 v235, v235, v183
	ds_read_b128 v[16:19], v178 offset:8192
	ds_read_b128 v[20:23], v178 offset:8208
	ds_read_b128 v[24:27], v178 offset:8224
	ds_read_b128 v[28:31], v178 offset:8240
	ds_read_b128 v[190:193], v178 offset:8256
	ds_read_b128 v[10:13], v178 offset:8272
	ds_read_b128 v[180:183], v178 offset:8288
	ds_read_b128 v[6:9], v178 offset:8304
	s_waitcnt lgkmcnt(0)
	v_add3_u32 v236, v16, v17, v18
	v_add3_u32 v19, v19, v20, v21
	v_add3_u32 v236, v236, v22, v23
	v_add_u32_e32 v236, v236, v19
	v_add3_u32 v237, v24, v25, v26
	v_add3_u32 v27, v27, v28, v29
	v_add3_u32 v237, v237, v30, v31
	v_add_u32_e32 v237, v237, v27
	v_add3_u32 v238, v190, v191, v192
	v_add3_u32 v193, v193, v10, v11
	v_add3_u32 v238, v238, v12, v13
	v_add_u32_e32 v238, v238, v193
	v_add3_u32 v239, v180, v181, v182
	v_add3_u32 v183, v183, v6, v7
	v_add3_u32 v239, v239, v8, v9
	v_add_u32_e32 v239, v239, v183
	v_add3_u32 v240, v232, v233, v234
	v_add3_u32 v241, v236, v237, v238
	v_add_u32_e32 v240, v240, v235
	v_add_u32_e32 v241, v241, v239
	v_lshl_add_u32 v242, v241, 16, v240
	s_nop 1
	v_add_u32_dpp v242, v242, v242 row_shr:1 row_mask:0xf bank_mask:0xf bound_ctrl:1
	s_nop 1
	v_add_u32_dpp v242, v242, v242 row_shr:2 row_mask:0xf bank_mask:0xf bound_ctrl:1
	s_nop 1
	v_add_u32_dpp v242, v242, v242 row_shr:4 row_mask:0xf bank_mask:0xf bound_ctrl:1
	s_nop 1
	v_add_u32_dpp v242, v242, v242 row_shr:8 row_mask:0xf bank_mask:0xf bound_ctrl:1
	s_nop 1
	v_add_u32_dpp v242, v242, v242 row_bcast:15 row_mask:0xa bank_mask:0xf
	s_nop 1
	v_add_u32_dpp v242, v242, v242 row_bcast:31 row_mask:0xc bank_mask:0xf
	s_nop 1
	v_readlane_b32 s20, v242, 63
	s_nop 1
	v_sub_u32_e32 v243, s20, v242
	v_and_b32_e32 v244, 0xffff, v243
	v_lshrrev_b32_e32 v246, 16, v243
	v_cmp_gt_u32_e64 s[58:59], s9, v244
	v_add_u32_e32 v245, v244, v240
	v_cmp_le_u32_e64 s[60:61], s9, v245
	s_and_b64 s[58:59], s[58:59], s[60:61]
	s_ff1_i32_b64 s21, s[58:59]
	s_and_b32 s21, s21, 63
	v_readlane_b32 s22, v244, s21
	v_readlane_b32 s23, v235, s21
	v_readlane_b32 s25, v234, s21
	v_readlane_b32 s26, v233, s21
	v_readlane_b32 s27, v232, s21
	s_add_u32 s28, s22, s23
	s_add_u32 s29, s28, s25
	s_add_u32 s32, s29, s26
	s_mov_b32 s37, 0
	s_mov_b32 s43, s27
	s_mov_b32 s85, s32
	s_cmp_le_u32 s9, s32
	s_cselect_b32 s37, 1, s37
	s_cselect_b32 s43, s26, s43
	s_cselect_b32 s85, s29, s85
	s_cmp_le_u32 s9, s29
	s_cselect_b32 s37, 2, s37
	s_cselect_b32 s43, s25, s43
	s_cselect_b32 s85, s28, s85
	s_cmp_le_u32 s9, s28
	s_cselect_b32 s37, 3, s37
	s_cselect_b32 s43, s23, s43
	s_cselect_b32 s85, s22, s85
	s_lshl_b32 s21, s21, 2
	s_add_i32 s21, s21, s37
	s_lshl_b32 s21, s21, s11
	s_or_b32 s21, s21, s7
	s_sub_i32 s22, s9, s85
	s_cmp_eq_u32 s43, s22
	s_cselect_b32 s23, 1, 0
	s_cmp_lg_u32 s12, 0
	s_cselect_b32 s7, s7, s21
	s_cselect_b32 s9, s9, s22
	s_cselect_b32 s12, 1, s23
	v_cmp_gt_u32_e64 s[58:59], s10, v246
	v_add_u32_e32 v245, v246, v241
	v_cmp_le_u32_e64 s[60:61], s10, v245
	s_and_b64 s[58:59], s[58:59], s[60:61]
	s_ff1_i32_b64 s21, s[58:59]
	s_and_b32 s21, s21, 63
	v_readlane_b32 s22, v246, s21
	v_readlane_b32 s23, v239, s21
	v_readlane_b32 s25, v238, s21
	v_readlane_b32 s26, v237, s21
	v_readlane_b32 s27, v236, s21
	s_add_u32 s28, s22, s23
	s_add_u32 s29, s28, s25
	s_add_u32 s32, s29, s26
	s_mov_b32 s37, 0
	s_mov_b32 s43, s27
	s_mov_b32 s85, s32
	s_cmp_le_u32 s10, s32
	s_cselect_b32 s37, 1, s37
	s_cselect_b32 s43, s26, s43
	s_cselect_b32 s85, s29, s85
	s_cmp_le_u32 s10, s29
	s_cselect_b32 s37, 2, s37
	s_cselect_b32 s43, s25, s43
	s_cselect_b32 s85, s28, s85
	s_cmp_le_u32 s10, s28
	s_cselect_b32 s37, 3, s37
	s_cselect_b32 s43, s23, s43
	s_cselect_b32 s85, s22, s85
	s_lshl_b32 s21, s21, 2
	s_add_i32 s21, s21, s37
	s_lshl_b32 s21, s21, s11
	s_or_b32 s21, s21, s8
	s_sub_i32 s22, s10, s85
	s_cmp_eq_u32 s43, s22
	s_cselect_b32 s23, 1, 0
	s_cmp_lg_u32 s13, 0
	s_cselect_b32 s8, s8, s21
	s_cselect_b32 s10, s10, s22
	s_cselect_b32 s13, 1, s23
	s_movk_i32 s11, 16
.Lsel_pass_12:
	s_and_b32 s20, s12, s13
	s_cmp_lg_u32 s20, 0
	s_cbranch_scc1 .Lsel_final_11
	ds_write_b128 v195, v[248:251]
	ds_write_b128 v195, v[248:251] offset:1280
	s_cmp_lg_u32 s12, 0
	s_cbranch_scc1 .Lsel_skip_ha_13
	s_cmp_lt_i32 s11, 16
	s_cbranch_scc1 .Lsel_latea_14
	v_xor_b32_e32 v9, s7, v200
	v_lshrrev_b32_e32 v9, s11, v9
	v_min_u32_e32 v9, v247, v9
	v_lshl_add_u32 v9, v9, 2, s5
	ds_add_u32 v9, v199
	v_xor_b32_e32 v10, s7, v201
	v_lshrrev_b32_e32 v10, s11, v10
	v_min_u32_e32 v10, v247, v10
	v_lshl_add_u32 v10, v10, 2, s5
	ds_add_u32 v10, v199
	v_xor_b32_e32 v11, s7, v202
	v_lshrrev_b32_e32 v11, s11, v11
	v_min_u32_e32 v11, v247, v11
	v_lshl_add_u32 v11, v11, 2, s5
	ds_add_u32 v11, v199
	v_xor_b32_e32 v12, s7, v203
	v_lshrrev_b32_e32 v12, s11, v12
	v_min_u32_e32 v12, v247, v12
	v_lshl_add_u32 v12, v12, 2, s5
	ds_add_u32 v12, v199
	v_xor_b32_e32 v9, s7, v204
	v_lshrrev_b32_e32 v9, s11, v9
	v_min_u32_e32 v9, v247, v9
	v_lshl_add_u32 v9, v9, 2, s5
	ds_add_u32 v9, v199
	v_xor_b32_e32 v10, s7, v205
	v_lshrrev_b32_e32 v10, s11, v10
	v_min_u32_e32 v10, v247, v10
	v_lshl_add_u32 v10, v10, 2, s5
	ds_add_u32 v10, v199
	v_xor_b32_e32 v11, s7, v206
	v_lshrrev_b32_e32 v11, s11, v11
	v_min_u32_e32 v11, v247, v11
	v_lshl_add_u32 v11, v11, 2, s5
	ds_add_u32 v11, v199
	v_xor_b32_e32 v12, s7, v207
	v_lshrrev_b32_e32 v12, s11, v12
	v_min_u32_e32 v12, v247, v12
	v_lshl_add_u32 v12, v12, 2, s5
	ds_add_u32 v12, v199
	s_cmp_lt_u32 s3, 8
	s_cbranch_scc1 .Lsel_pna_done_15
	v_xor_b32_e32 v9, s7, v208
	v_lshrrev_b32_e32 v9, s11, v9
	v_min_u32_e32 v9, v247, v9
	v_lshl_add_u32 v9, v9, 2, s5
	ds_add_u32 v9, v199
	v_xor_b32_e32 v10, s7, v209
	v_lshrrev_b32_e32 v10, s11, v10
	v_min_u32_e32 v10, v247, v10
	v_lshl_add_u32 v10, v10, 2, s5
	ds_add_u32 v10, v199
	v_xor_b32_e32 v11, s7, v210
	v_lshrrev_b32_e32 v11, s11, v11
	v_min_u32_e32 v11, v247, v11
	v_lshl_add_u32 v11, v11, 2, s5
	ds_add_u32 v11, v199
	v_xor_b32_e32 v12, s7, v211
	v_lshrrev_b32_e32 v12, s11, v12
	v_min_u32_e32 v12, v247, v12
	v_lshl_add_u32 v12, v12, 2, s5
	ds_add_u32 v12, v199
	s_cmp_lt_u32 s3, 12
	s_cbranch_scc1 .Lsel_pna_done_15
	v_xor_b32_e32 v9, s7, v212
	v_lshrrev_b32_e32 v9, s11, v9
	v_min_u32_e32 v9, v247, v9
	v_lshl_add_u32 v9, v9, 2, s5
	ds_add_u32 v9, v199
	v_xor_b32_e32 v10, s7, v213
	v_lshrrev_b32_e32 v10, s11, v10
	v_min_u32_e32 v10, v247, v10
	v_lshl_add_u32 v10, v10, 2, s5
	ds_add_u32 v10, v199
	v_xor_b32_e32 v11, s7, v214
	v_lshrrev_b32_e32 v11, s11, v11
	v_min_u32_e32 v11, v247, v11
	v_lshl_add_u32 v11, v11, 2, s5
	ds_add_u32 v11, v199
	v_xor_b32_e32 v12, s7, v215
	v_lshrrev_b32_e32 v12, s11, v12
	v_min_u32_e32 v12, v247, v12
	v_lshl_add_u32 v12, v12, 2, s5
	ds_add_u32 v12, v199
	s_cmp_lt_u32 s3, 16
	s_cbranch_scc1 .Lsel_pna_done_15
	v_xor_b32_e32 v9, s7, v216
	v_lshrrev_b32_e32 v9, s11, v9
	v_min_u32_e32 v9, v247, v9
	v_lshl_add_u32 v9, v9, 2, s5
	ds_add_u32 v9, v199
	v_xor_b32_e32 v10, s7, v217
	v_lshrrev_b32_e32 v10, s11, v10
	v_min_u32_e32 v10, v247, v10
	v_lshl_add_u32 v10, v10, 2, s5
	ds_add_u32 v10, v199
	v_xor_b32_e32 v11, s7, v218
	v_lshrrev_b32_e32 v11, s11, v11
	v_min_u32_e32 v11, v247, v11
	v_lshl_add_u32 v11, v11, 2, s5
	ds_add_u32 v11, v199
	v_xor_b32_e32 v12, s7, v219
	v_lshrrev_b32_e32 v12, s11, v12
	v_min_u32_e32 v12, v247, v12
	v_lshl_add_u32 v12, v12, 2, s5
	ds_add_u32 v12, v199
	s_cmp_lt_u32 s3, 20
	s_cbranch_scc1 .Lsel_pna_done_15
	v_xor_b32_e32 v9, s7, v220
	v_lshrrev_b32_e32 v9, s11, v9
	v_min_u32_e32 v9, v247, v9
	v_lshl_add_u32 v9, v9, 2, s5
	ds_add_u32 v9, v199
	v_xor_b32_e32 v10, s7, v221
	v_lshrrev_b32_e32 v10, s11, v10
	v_min_u32_e32 v10, v247, v10
	v_lshl_add_u32 v10, v10, 2, s5
	ds_add_u32 v10, v199
	v_xor_b32_e32 v11, s7, v222
	v_lshrrev_b32_e32 v11, s11, v11
	v_min_u32_e32 v11, v247, v11
	v_lshl_add_u32 v11, v11, 2, s5
	ds_add_u32 v11, v199
	v_xor_b32_e32 v12, s7, v223
	v_lshrrev_b32_e32 v12, s11, v12
	v_min_u32_e32 v12, v247, v12
	v_lshl_add_u32 v12, v12, 2, s5
	ds_add_u32 v12, v199
	s_cmp_lt_u32 s3, 24
	s_cbranch_scc1 .Lsel_pna_done_15
	v_xor_b32_e32 v9, s7, v224
	v_lshrrev_b32_e32 v9, s11, v9
	v_min_u32_e32 v9, v247, v9
	v_lshl_add_u32 v9, v9, 2, s5
	ds_add_u32 v9, v199
	v_xor_b32_e32 v10, s7, v225
	v_lshrrev_b32_e32 v10, s11, v10
	v_min_u32_e32 v10, v247, v10
	v_lshl_add_u32 v10, v10, 2, s5
	ds_add_u32 v10, v199
	v_xor_b32_e32 v11, s7, v226
	v_lshrrev_b32_e32 v11, s11, v11
	v_min_u32_e32 v11, v247, v11
	v_lshl_add_u32 v11, v11, 2, s5
	ds_add_u32 v11, v199
	v_xor_b32_e32 v12, s7, v227
	v_lshrrev_b32_e32 v12, s11, v12
	v_min_u32_e32 v12, v247, v12
	v_lshl_add_u32 v12, v12, 2, s5
	ds_add_u32 v12, v199
	s_cmp_lt_u32 s3, 28
	s_cbranch_scc1 .Lsel_pna_done_15
	v_xor_b32_e32 v9, s7, v228
	v_lshrrev_b32_e32 v9, s11, v9
	v_min_u32_e32 v9, v247, v9
	v_lshl_add_u32 v9, v9, 2, s5
	ds_add_u32 v9, v199
	v_xor_b32_e32 v10, s7, v229
	v_lshrrev_b32_e32 v10, s11, v10
	v_min_u32_e32 v10, v247, v10
	v_lshl_add_u32 v10, v10, 2, s5
	ds_add_u32 v10, v199
	v_xor_b32_e32 v11, s7, v230
	v_lshrrev_b32_e32 v11, s11, v11
	v_min_u32_e32 v11, v247, v11
	v_lshl_add_u32 v11, v11, 2, s5
	ds_add_u32 v11, v199
	v_xor_b32_e32 v12, s7, v231
	v_lshrrev_b32_e32 v12, s11, v12
	v_min_u32_e32 v12, v247, v12
	v_lshl_add_u32 v12, v12, 2, s5
	ds_add_u32 v12, v199

.Lsel_latea_14:
	s_movk_i32 s20, 0x100
	v_xor_b32_e32 v9, s7, v200
	v_lshrrev_b32_e32 v9, s11, v9
	v_xor_b32_e32 v10, s7, v201
	v_lshrrev_b32_e32 v10, s11, v10
	v_xor_b32_e32 v11, s7, v202
	v_lshrrev_b32_e32 v11, s11, v11
	v_xor_b32_e32 v12, s7, v203
	v_lshrrev_b32_e32 v12, s11, v12
	v_min3_u32 v13, v9, v10, v11
	v_min_u32_e32 v13, v13, v12
	v_cmp_gt_u32_e32 vcc, s20, v13
	s_cbranch_vccz .Lsel_nc_17
	v_min_u32_e32 v9, v247, v9
	v_lshl_add_u32 v9, v9, 2, s5
	ds_add_u32 v9, v199
	v_min_u32_e32 v10, v247, v10
	v_lshl_add_u32 v10, v10, 2, s5
	ds_add_u32 v10, v199
	v_min_u32_e32 v11, v247, v11
	v_lshl_add_u32 v11, v11, 2, s5
	ds_add_u32 v11, v199
	v_min_u32_e32 v12, v247, v12
	v_lshl_add_u32 v12, v12, 2, s5
	ds_add_u32 v12, v199
.Lsel_nc_17:
	v_xor_b32_e32 v9, s7, v204
	v_lshrrev_b32_e32 v9, s11, v9
	v_xor_b32_e32 v10, s7, v205
	v_lshrrev_b32_e32 v10, s11, v10
	v_xor_b32_e32 v11, s7, v206
	v_lshrrev_b32_e32 v11, s11, v11
	v_xor_b32_e32 v12, s7, v207
	v_lshrrev_b32_e32 v12, s11, v12
	v_min3_u32 v13, v9, v10, v11
	v_min_u32_e32 v13, v13, v12
	v_cmp_gt_u32_e32 vcc, s20, v13
	s_cbranch_vccz .Lsel_nc_18
	v_min_u32_e32 v9, v247, v9
	v_lshl_add_u32 v9, v9, 2, s5
	ds_add_u32 v9, v199
	v_min_u32_e32 v10, v247, v10
	v_lshl_add_u32 v10, v10, 2, s5
	ds_add_u32 v10, v199
	v_min_u32_e32 v11, v247, v11
	v_lshl_add_u32 v11, v11, 2, s5
	ds_add_u32 v11, v199
	v_min_u32_e32 v12, v247, v12
	v_lshl_add_u32 v12, v12, 2, s5
	ds_add_u32 v12, v199
.Lsel_nc_18:
	s_cmp_lt_u32 s3, 8
	s_cbranch_scc1 .Lsel_psa_done_16
	v_xor_b32_e32 v9, s7, v208
	v_lshrrev_b32_e32 v9, s11, v9
	v_xor_b32_e32 v10, s7, v209
	v_lshrrev_b32_e32 v10, s11, v10
	v_xor_b32_e32 v11, s7, v210
	v_lshrrev_b32_e32 v11, s11, v11
	v_xor_b32_e32 v12, s7, v211
	v_lshrrev_b32_e32 v12, s11, v12
	v_min3_u32 v13, v9, v10, v11
	v_min_u32_e32 v13, v13, v12
	v_cmp_gt_u32_e32 vcc, s20, v13
	s_cbranch_vccz .Lsel_nc_19
	v_min_u32_e32 v9, v247, v9
	v_lshl_add_u32 v9, v9, 2, s5
	ds_add_u32 v9, v199
	v_min_u32_e32 v10, v247, v10
	v_lshl_add_u32 v10, v10, 2, s5
	ds_add_u32 v10, v199
	v_min_u32_e32 v11, v247, v11
	v_lshl_add_u32 v11, v11, 2, s5
	ds_add_u32 v11, v199
	v_min_u32_e32 v12, v247, v12
	v_lshl_add_u32 v12, v12, 2, s5
	ds_add_u32 v12, v199
.Lsel_nc_19:
	s_cmp_lt_u32 s3, 12
	s_cbranch_scc1 .Lsel_psa_done_16
	v_xor_b32_e32 v9, s7, v212
	v_lshrrev_b32_e32 v9, s11, v9
	v_xor_b32_e32 v10, s7, v213
	v_lshrrev_b32_e32 v10, s11, v10
	v_xor_b32_e32 v11, s7, v214
	v_lshrrev_b32_e32 v11, s11, v11
	v_xor_b32_e32 v12, s7, v215
	v_lshrrev_b32_e32 v12, s11, v12
	v_min3_u32 v13, v9, v10, v11
	v_min_u32_e32 v13, v13, v12
	v_cmp_gt_u32_e32 vcc, s20, v13
	s_cbranch_vccz .Lsel_nc_20
	v_min_u32_e32 v9, v247, v9
	v_lshl_add_u32 v9, v9, 2, s5
	ds_add_u32 v9, v199
	v_min_u32_e32 v10, v247, v10
	v_lshl_add_u32 v10, v10, 2, s5
	ds_add_u32 v10, v199
	v_min_u32_e32 v11, v247, v11
	v_lshl_add_u32 v11, v11, 2, s5
	ds_add_u32 v11, v199
	v_min_u32_e32 v12, v247, v12
	v_lshl_add_u32 v12, v12, 2, s5
	ds_add_u32 v12, v199
.Lsel_nc_20:
	s_cmp_lt_u32 s3, 16
	s_cbranch_scc1 .Lsel_psa_done_16
	v_xor_b32_e32 v9, s7, v216
	v_lshrrev_b32_e32 v9, s11, v9
	v_xor_b32_e32 v10, s7, v217
	v_lshrrev_b32_e32 v10, s11, v10
	v_xor_b32_e32 v11, s7, v218
	v_lshrrev_b32_e32 v11, s11, v11
	v_xor_b32_e32 v12, s7, v219
	v_lshrrev_b32_e32 v12, s11, v12
	v_min3_u32 v13, v9, v10, v11
	v_min_u32_e32 v13, v13, v12
	v_cmp_gt_u32_e32 vcc, s20, v13
	s_cbranch_vccz .Lsel_nc_21
	v_min_u32_e32 v9, v247, v9
	v_lshl_add_u32 v9, v9, 2, s5
	ds_add_u32 v9, v199
	v_min_u32_e32 v10, v247, v10
	v_lshl_add_u32 v10, v10, 2, s5
	ds_add_u32 v10, v199
	v_min_u32_e32 v11, v247, v11
	v_lshl_add_u32 v11, v11, 2, s5
	ds_add_u32 v11, v199
	v_min_u32_e32 v12, v247, v12
	v_lshl_add_u32 v12, v12, 2, s5
	ds_add_u32 v12, v199
.Lsel_nc_21:
	s_cmp_lt_u32 s3, 20
	s_cbranch_scc1 .Lsel_psa_done_16
	v_xor_b32_e32 v9, s7, v220
	v_lshrrev_b32_e32 v9, s11, v9
	v_xor_b32_e32 v10, s7, v221
	v_lshrrev_b32_e32 v10, s11, v10
	v_xor_b32_e32 v11, s7, v222
	v_lshrrev_b32_e32 v11, s11, v11
	v_xor_b32_e32 v12, s7, v223
	v_lshrrev_b32_e32 v12, s11, v12
	v_min3_u32 v13, v9, v10, v11
	v_min_u32_e32 v13, v13, v12
	v_cmp_gt_u32_e32 vcc, s20, v13
	s_cbranch_vccz .Lsel_nc_22
	v_min_u32_e32 v9, v247, v9
	v_lshl_add_u32 v9, v9, 2, s5
	ds_add_u32 v9, v199
	v_min_u32_e32 v10, v247, v10
	v_lshl_add_u32 v10, v10, 2, s5
	ds_add_u32 v10, v199
	v_min_u32_e32 v11, v247, v11
	v_lshl_add_u32 v11, v11, 2, s5
	ds_add_u32 v11, v199
	v_min_u32_e32 v12, v247, v12
	v_lshl_add_u32 v12, v12, 2, s5
	ds_add_u32 v12, v199
.Lsel_nc_22:
	s_cmp_lt_u32 s3, 24
	s_cbranch_scc1 .Lsel_psa_done_16
	v_xor_b32_e32 v9, s7, v224
	v_lshrrev_b32_e32 v9, s11, v9
	v_xor_b32_e32 v10, s7, v225
	v_lshrrev_b32_e32 v10, s11, v10
	v_xor_b32_e32 v11, s7, v226
	v_lshrrev_b32_e32 v11, s11, v11
	v_xor_b32_e32 v12, s7, v227
	v_lshrrev_b32_e32 v12, s11, v12
	v_min3_u32 v13, v9, v10, v11
	v_min_u32_e32 v13, v13, v12
	v_cmp_gt_u32_e32 vcc, s20, v13
	s_cbranch_vccz .Lsel_nc_23
	v_min_u32_e32 v9, v247, v9
	v_lshl_add_u32 v9, v9, 2, s5
	ds_add_u32 v9, v199
	v_min_u32_e32 v10, v247, v10
	v_lshl_add_u32 v10, v10, 2, s5
	ds_add_u32 v10, v199
	v_min_u32_e32 v11, v247, v11
	v_lshl_add_u32 v11, v11, 2, s5
	ds_add_u32 v11, v199
	v_min_u32_e32 v12, v247, v12
	v_lshl_add_u32 v12, v12, 2, s5
	ds_add_u32 v12, v199
.Lsel_nc_23:
	s_cmp_lt_u32 s3, 28
	s_cbranch_scc1 .Lsel_psa_done_16
	v_xor_b32_e32 v9, s7, v228
	v_lshrrev_b32_e32 v9, s11, v9
	v_xor_b32_e32 v10, s7, v229
	v_lshrrev_b32_e32 v10, s11, v10
	v_xor_b32_e32 v11, s7, v230
	v_lshrrev_b32_e32 v11, s11, v11
	v_xor_b32_e32 v12, s7, v231
	v_lshrrev_b32_e32 v12, s11, v12
	v_min3_u32 v13, v9, v10, v11
	v_min_u32_e32 v13, v13, v12
	v_cmp_gt_u32_e32 vcc, s20, v13
	s_cbranch_vccz .Lsel_nc_24
	v_min_u32_e32 v9, v247, v9
	v_lshl_add_u32 v9, v9, 2, s5
	ds_add_u32 v9, v199
	v_min_u32_e32 v10, v247, v10
	v_lshl_add_u32 v10, v10, 2, s5
	ds_add_u32 v10, v199
	v_min_u32_e32 v11, v247, v11
	v_lshl_add_u32 v11, v11, 2, s5
	ds_add_u32 v11, v199
	v_min_u32_e32 v12, v247, v12
	v_lshl_add_u32 v12, v12, 2, s5
	ds_add_u32 v12, v199
.Lsel_nc_24:
.Lsel_psa_done_16:
.Lsel_skip_ha_13:
	s_cmp_lg_u32 s13, 0
	s_cbranch_scc1 .Lsel_skip_hb_25
	s_cmp_lt_i32 s11, 16
	s_cbranch_scc1 .Lsel_lateb_26
	v_xor_b32_e32 v9, s8, v148
	v_lshrrev_b32_e32 v9, s11, v9
	v_min_u32_e32 v9, v247, v9
	v_lshl_add_u32 v9, v9, 2, s6
	ds_add_u32 v9, v199
	v_xor_b32_e32 v10, s8, v149
	v_lshrrev_b32_e32 v10, s11, v10
	v_min_u32_e32 v10, v247, v10
	v_lshl_add_u32 v10, v10, 2, s6
	ds_add_u32 v10, v199
	v_xor_b32_e32 v11, s8, v150
	v_lshrrev_b32_e32 v11, s11, v11
	v_min_u32_e32 v11, v247, v11
	v_lshl_add_u32 v11, v11, 2, s6
	ds_add_u32 v11, v199
	v_xor_b32_e32 v12, s8, v151
	v_lshrrev_b32_e32 v12, s11, v12
	v_min_u32_e32 v12, v247, v12
	v_lshl_add_u32 v12, v12, 2, s6
	ds_add_u32 v12, v199
	v_xor_b32_e32 v9, s8, v152
	v_lshrrev_b32_e32 v9, s11, v9
	v_min_u32_e32 v9, v247, v9
	v_lshl_add_u32 v9, v9, 2, s6
	ds_add_u32 v9, v199
	v_xor_b32_e32 v10, s8, v153
	v_lshrrev_b32_e32 v10, s11, v10
	v_min_u32_e32 v10, v247, v10
	v_lshl_add_u32 v10, v10, 2, s6
	ds_add_u32 v10, v199
	v_xor_b32_e32 v11, s8, v154
	v_lshrrev_b32_e32 v11, s11, v11
	v_min_u32_e32 v11, v247, v11
	v_lshl_add_u32 v11, v11, 2, s6
	ds_add_u32 v11, v199
	v_xor_b32_e32 v12, s8, v155
	v_lshrrev_b32_e32 v12, s11, v12
	v_min_u32_e32 v12, v247, v12
	v_lshl_add_u32 v12, v12, 2, s6
	ds_add_u32 v12, v199
	s_cmp_lt_u32 s3, 8
	s_cbranch_scc1 .Lsel_pnb_done_27
	v_xor_b32_e32 v9, s8, v156
	v_lshrrev_b32_e32 v9, s11, v9
	v_min_u32_e32 v9, v247, v9
	v_lshl_add_u32 v9, v9, 2, s6
	ds_add_u32 v9, v199
	v_xor_b32_e32 v10, s8, v157
	v_lshrrev_b32_e32 v10, s11, v10
	v_min_u32_e32 v10, v247, v10
	v_lshl_add_u32 v10, v10, 2, s6
	ds_add_u32 v10, v199
	v_xor_b32_e32 v11, s8, v158
	v_lshrrev_b32_e32 v11, s11, v11
	v_min_u32_e32 v11, v247, v11
	v_lshl_add_u32 v11, v11, 2, s6
	ds_add_u32 v11, v199
	v_xor_b32_e32 v12, s8, v159
	v_lshrrev_b32_e32 v12, s11, v12
	v_min_u32_e32 v12, v247, v12
	v_lshl_add_u32 v12, v12, 2, s6
	ds_add_u32 v12, v199
	s_cmp_lt_u32 s3, 12
	s_cbranch_scc1 .Lsel_pnb_done_27
	v_xor_b32_e32 v9, s8, v160
	v_lshrrev_b32_e32 v9, s11, v9
	v_min_u32_e32 v9, v247, v9
	v_lshl_add_u32 v9, v9, 2, s6
	ds_add_u32 v9, v199
	v_xor_b32_e32 v10, s8, v161
	v_lshrrev_b32_e32 v10, s11, v10
	v_min_u32_e32 v10, v247, v10
	v_lshl_add_u32 v10, v10, 2, s6
	ds_add_u32 v10, v199
	v_xor_b32_e32 v11, s8, v162
	v_lshrrev_b32_e32 v11, s11, v11
	v_min_u32_e32 v11, v247, v11
	v_lshl_add_u32 v11, v11, 2, s6
	ds_add_u32 v11, v199
	v_xor_b32_e32 v12, s8, v163
	v_lshrrev_b32_e32 v12, s11, v12
	v_min_u32_e32 v12, v247, v12
	v_lshl_add_u32 v12, v12, 2, s6
	ds_add_u32 v12, v199
	s_cmp_lt_u32 s3, 16
	s_cbranch_scc1 .Lsel_pnb_done_27
	v_xor_b32_e32 v9, s8, v164
	v_lshrrev_b32_e32 v9, s11, v9
	v_min_u32_e32 v9, v247, v9
	v_lshl_add_u32 v9, v9, 2, s6
	ds_add_u32 v9, v199
	v_xor_b32_e32 v10, s8, v165
	v_lshrrev_b32_e32 v10, s11, v10
	v_min_u32_e32 v10, v247, v10
	v_lshl_add_u32 v10, v10, 2, s6
	ds_add_u32 v10, v199
	v_xor_b32_e32 v11, s8, v166
	v_lshrrev_b32_e32 v11, s11, v11
	v_min_u32_e32 v11, v247, v11
	v_lshl_add_u32 v11, v11, 2, s6
	ds_add_u32 v11, v199
	v_xor_b32_e32 v12, s8, v167
	v_lshrrev_b32_e32 v12, s11, v12
	v_min_u32_e32 v12, v247, v12
	v_lshl_add_u32 v12, v12, 2, s6
	ds_add_u32 v12, v199
	s_cmp_lt_u32 s3, 20
	s_cbranch_scc1 .Lsel_pnb_done_27
	v_xor_b32_e32 v9, s8, v168
	v_lshrrev_b32_e32 v9, s11, v9
	v_min_u32_e32 v9, v247, v9
	v_lshl_add_u32 v9, v9, 2, s6
	ds_add_u32 v9, v199
	v_xor_b32_e32 v10, s8, v169
	v_lshrrev_b32_e32 v10, s11, v10
	v_min_u32_e32 v10, v247, v10
	v_lshl_add_u32 v10, v10, 2, s6
	ds_add_u32 v10, v199
	v_xor_b32_e32 v11, s8, v170
	v_lshrrev_b32_e32 v11, s11, v11
	v_min_u32_e32 v11, v247, v11
	v_lshl_add_u32 v11, v11, 2, s6
	ds_add_u32 v11, v199
	v_xor_b32_e32 v12, s8, v171
	v_lshrrev_b32_e32 v12, s11, v12
	v_min_u32_e32 v12, v247, v12
	v_lshl_add_u32 v12, v12, 2, s6
	ds_add_u32 v12, v199
	s_cmp_lt_u32 s3, 24
	s_cbranch_scc1 .Lsel_pnb_done_27
	v_xor_b32_e32 v9, s8, v172
	v_lshrrev_b32_e32 v9, s11, v9
	v_min_u32_e32 v9, v247, v9
	v_lshl_add_u32 v9, v9, 2, s6
	ds_add_u32 v9, v199
	v_xor_b32_e32 v10, s8, v173
	v_lshrrev_b32_e32 v10, s11, v10
	v_min_u32_e32 v10, v247, v10
	v_lshl_add_u32 v10, v10, 2, s6
	ds_add_u32 v10, v199
	v_xor_b32_e32 v11, s8, v174
	v_lshrrev_b32_e32 v11, s11, v11
	v_min_u32_e32 v11, v247, v11
	v_lshl_add_u32 v11, v11, 2, s6
	ds_add_u32 v11, v199
	v_xor_b32_e32 v12, s8, v175
	v_lshrrev_b32_e32 v12, s11, v12
	v_min_u32_e32 v12, v247, v12
	v_lshl_add_u32 v12, v12, 2, s6
	ds_add_u32 v12, v199
	s_cmp_lt_u32 s3, 28
	s_cbranch_scc1 .Lsel_pnb_done_27
	v_xor_b32_e32 v9, s8, v176
	v_lshrrev_b32_e32 v9, s11, v9
	v_min_u32_e32 v9, v247, v9
	v_lshl_add_u32 v9, v9, 2, s6
	ds_add_u32 v9, v199
	v_xor_b32_e32 v10, s8, v177
	v_lshrrev_b32_e32 v10, s11, v10
	v_min_u32_e32 v10, v247, v10
	v_lshl_add_u32 v10, v10, 2, s6
	ds_add_u32 v10, v199
	v_xor_b32_e32 v11, s8, v186
	v_lshrrev_b32_e32 v11, s11, v11
	v_min_u32_e32 v11, v247, v11
	v_lshl_add_u32 v11, v11, 2, s6
	ds_add_u32 v11, v199
	v_xor_b32_e32 v12, s8, v187
	v_lshrrev_b32_e32 v12, s11, v12
	v_min_u32_e32 v12, v247, v12
	v_lshl_add_u32 v12, v12, 2, s6
	ds_add_u32 v12, v199

.Lsel_lateb_26:
	s_movk_i32 s20, 0x100
	v_xor_b32_e32 v9, s8, v148
	v_lshrrev_b32_e32 v9, s11, v9
	v_xor_b32_e32 v10, s8, v149
	v_lshrrev_b32_e32 v10, s11, v10
	v_xor_b32_e32 v11, s8, v150
	v_lshrrev_b32_e32 v11, s11, v11
	v_xor_b32_e32 v12, s8, v151
	v_lshrrev_b32_e32 v12, s11, v12
	v_min3_u32 v13, v9, v10, v11
	v_min_u32_e32 v13, v13, v12
	v_cmp_gt_u32_e32 vcc, s20, v13
	s_cbranch_vccz .Lsel_nc_29
	v_min_u32_e32 v9, v247, v9
	v_lshl_add_u32 v9, v9, 2, s6
	ds_add_u32 v9, v199
	v_min_u32_e32 v10, v247, v10
	v_lshl_add_u32 v10, v10, 2, s6
	ds_add_u32 v10, v199
	v_min_u32_e32 v11, v247, v11
	v_lshl_add_u32 v11, v11, 2, s6
	ds_add_u32 v11, v199
	v_min_u32_e32 v12, v247, v12
	v_lshl_add_u32 v12, v12, 2, s6
	ds_add_u32 v12, v199
.Lsel_nc_29:
	v_xor_b32_e32 v9, s8, v152
	v_lshrrev_b32_e32 v9, s11, v9
	v_xor_b32_e32 v10, s8, v153
	v_lshrrev_b32_e32 v10, s11, v10
	v_xor_b32_e32 v11, s8, v154
	v_lshrrev_b32_e32 v11, s11, v11
	v_xor_b32_e32 v12, s8, v155
	v_lshrrev_b32_e32 v12, s11, v12
	v_min3_u32 v13, v9, v10, v11
	v_min_u32_e32 v13, v13, v12
	v_cmp_gt_u32_e32 vcc, s20, v13
	s_cbranch_vccz .Lsel_nc_30
	v_min_u32_e32 v9, v247, v9
	v_lshl_add_u32 v9, v9, 2, s6
	ds_add_u32 v9, v199
	v_min_u32_e32 v10, v247, v10
	v_lshl_add_u32 v10, v10, 2, s6
	ds_add_u32 v10, v199
	v_min_u32_e32 v11, v247, v11
	v_lshl_add_u32 v11, v11, 2, s6
	ds_add_u32 v11, v199
	v_min_u32_e32 v12, v247, v12
	v_lshl_add_u32 v12, v12, 2, s6
	ds_add_u32 v12, v199
.Lsel_nc_30:
	s_cmp_lt_u32 s3, 8
	s_cbranch_scc1 .Lsel_psb_done_28
	v_xor_b32_e32 v9, s8, v156
	v_lshrrev_b32_e32 v9, s11, v9
	v_xor_b32_e32 v10, s8, v157
	v_lshrrev_b32_e32 v10, s11, v10
	v_xor_b32_e32 v11, s8, v158
	v_lshrrev_b32_e32 v11, s11, v11
	v_xor_b32_e32 v12, s8, v159
	v_lshrrev_b32_e32 v12, s11, v12
	v_min3_u32 v13, v9, v10, v11
	v_min_u32_e32 v13, v13, v12
	v_cmp_gt_u32_e32 vcc, s20, v13
	s_cbranch_vccz .Lsel_nc_31
	v_min_u32_e32 v9, v247, v9
	v_lshl_add_u32 v9, v9, 2, s6
	ds_add_u32 v9, v199
	v_min_u32_e32 v10, v247, v10
	v_lshl_add_u32 v10, v10, 2, s6
	ds_add_u32 v10, v199
	v_min_u32_e32 v11, v247, v11
	v_lshl_add_u32 v11, v11, 2, s6
	ds_add_u32 v11, v199
	v_min_u32_e32 v12, v247, v12
	v_lshl_add_u32 v12, v12, 2, s6
	ds_add_u32 v12, v199
.Lsel_nc_31:
	s_cmp_lt_u32 s3, 12
	s_cbranch_scc1 .Lsel_psb_done_28
	v_xor_b32_e32 v9, s8, v160
	v_lshrrev_b32_e32 v9, s11, v9
	v_xor_b32_e32 v10, s8, v161
	v_lshrrev_b32_e32 v10, s11, v10
	v_xor_b32_e32 v11, s8, v162
	v_lshrrev_b32_e32 v11, s11, v11
	v_xor_b32_e32 v12, s8, v163
	v_lshrrev_b32_e32 v12, s11, v12
	v_min3_u32 v13, v9, v10, v11
	v_min_u32_e32 v13, v13, v12
	v_cmp_gt_u32_e32 vcc, s20, v13
	s_cbranch_vccz .Lsel_nc_32
	v_min_u32_e32 v9, v247, v9
	v_lshl_add_u32 v9, v9, 2, s6
	ds_add_u32 v9, v199
	v_min_u32_e32 v10, v247, v10
	v_lshl_add_u32 v10, v10, 2, s6
	ds_add_u32 v10, v199
	v_min_u32_e32 v11, v247, v11
	v_lshl_add_u32 v11, v11, 2, s6
	ds_add_u32 v11, v199
	v_min_u32_e32 v12, v247, v12
	v_lshl_add_u32 v12, v12, 2, s6
	ds_add_u32 v12, v199
.Lsel_nc_32:
	s_cmp_lt_u32 s3, 16
	s_cbranch_scc1 .Lsel_psb_done_28
	v_xor_b32_e32 v9, s8, v164
	v_lshrrev_b32_e32 v9, s11, v9
	v_xor_b32_e32 v10, s8, v165
	v_lshrrev_b32_e32 v10, s11, v10
	v_xor_b32_e32 v11, s8, v166
	v_lshrrev_b32_e32 v11, s11, v11
	v_xor_b32_e32 v12, s8, v167
	v_lshrrev_b32_e32 v12, s11, v12
	v_min3_u32 v13, v9, v10, v11
	v_min_u32_e32 v13, v13, v12
	v_cmp_gt_u32_e32 vcc, s20, v13
	s_cbranch_vccz .Lsel_nc_33
	v_min_u32_e32 v9, v247, v9
	v_lshl_add_u32 v9, v9, 2, s6
	ds_add_u32 v9, v199
	v_min_u32_e32 v10, v247, v10
	v_lshl_add_u32 v10, v10, 2, s6
	ds_add_u32 v10, v199
	v_min_u32_e32 v11, v247, v11
	v_lshl_add_u32 v11, v11, 2, s6
	ds_add_u32 v11, v199
	v_min_u32_e32 v12, v247, v12
	v_lshl_add_u32 v12, v12, 2, s6
	ds_add_u32 v12, v199
.Lsel_nc_33:
	s_cmp_lt_u32 s3, 20
	s_cbranch_scc1 .Lsel_psb_done_28
	v_xor_b32_e32 v9, s8, v168
	v_lshrrev_b32_e32 v9, s11, v9
	v_xor_b32_e32 v10, s8, v169
	v_lshrrev_b32_e32 v10, s11, v10
	v_xor_b32_e32 v11, s8, v170
	v_lshrrev_b32_e32 v11, s11, v11
	v_xor_b32_e32 v12, s8, v171
	v_lshrrev_b32_e32 v12, s11, v12
	v_min3_u32 v13, v9, v10, v11
	v_min_u32_e32 v13, v13, v12
	v_cmp_gt_u32_e32 vcc, s20, v13
	s_cbranch_vccz .Lsel_nc_34
	v_min_u32_e32 v9, v247, v9
	v_lshl_add_u32 v9, v9, 2, s6
	ds_add_u32 v9, v199
	v_min_u32_e32 v10, v247, v10
	v_lshl_add_u32 v10, v10, 2, s6
	ds_add_u32 v10, v199
	v_min_u32_e32 v11, v247, v11
	v_lshl_add_u32 v11, v11, 2, s6
	ds_add_u32 v11, v199
	v_min_u32_e32 v12, v247, v12
	v_lshl_add_u32 v12, v12, 2, s6
	ds_add_u32 v12, v199
.Lsel_nc_34:
	s_cmp_lt_u32 s3, 24
	s_cbranch_scc1 .Lsel_psb_done_28
	v_xor_b32_e32 v9, s8, v172
	v_lshrrev_b32_e32 v9, s11, v9
	v_xor_b32_e32 v10, s8, v173
	v_lshrrev_b32_e32 v10, s11, v10
	v_xor_b32_e32 v11, s8, v174
	v_lshrrev_b32_e32 v11, s11, v11
	v_xor_b32_e32 v12, s8, v175
	v_lshrrev_b32_e32 v12, s11, v12
	v_min3_u32 v13, v9, v10, v11
	v_min_u32_e32 v13, v13, v12
	v_cmp_gt_u32_e32 vcc, s20, v13
	s_cbranch_vccz .Lsel_nc_35
	v_min_u32_e32 v9, v247, v9
	v_lshl_add_u32 v9, v9, 2, s6
	ds_add_u32 v9, v199
	v_min_u32_e32 v10, v247, v10
	v_lshl_add_u32 v10, v10, 2, s6
	ds_add_u32 v10, v199
	v_min_u32_e32 v11, v247, v11
	v_lshl_add_u32 v11, v11, 2, s6
	ds_add_u32 v11, v199
	v_min_u32_e32 v12, v247, v12
	v_lshl_add_u32 v12, v12, 2, s6
	ds_add_u32 v12, v199
.Lsel_nc_35:
	s_cmp_lt_u32 s3, 28
	s_cbranch_scc1 .Lsel_psb_done_28
	v_xor_b32_e32 v9, s8, v176
	v_lshrrev_b32_e32 v9, s11, v9
	v_xor_b32_e32 v10, s8, v177
	v_lshrrev_b32_e32 v10, s11, v10
	v_xor_b32_e32 v11, s8, v186
	v_lshrrev_b32_e32 v11, s11, v11
	v_xor_b32_e32 v12, s8, v187
	v_lshrrev_b32_e32 v12, s11, v12
	v_min3_u32 v13, v9, v10, v11
	v_min_u32_e32 v13, v13, v12
	v_cmp_gt_u32_e32 vcc, s20, v13
	s_cbranch_vccz .Lsel_nc_36
	v_min_u32_e32 v9, v247, v9
	v_lshl_add_u32 v9, v9, 2, s6
	ds_add_u32 v9, v199
	v_min_u32_e32 v10, v247, v10
	v_lshl_add_u32 v10, v10, 2, s6
	ds_add_u32 v10, v199
	v_min_u32_e32 v11, v247, v11
	v_lshl_add_u32 v11, v11, 2, s6
	ds_add_u32 v11, v199
	v_min_u32_e32 v12, v247, v12
	v_lshl_add_u32 v12, v12, 2, s6
	ds_add_u32 v12, v199
.Lsel_nc_36:
.Lsel_psb_done_28:
.Lsel_skip_hb_25:
	s_waitcnt lgkmcnt(0)
	ds_read_b128 v[232:235], v195
	ds_read_b128 v[236:239], v195 offset:1280
	s_waitcnt lgkmcnt(0)
	v_add3_u32 v240, v232, v233, v234
	v_add3_u32 v241, v236, v237, v238
	v_add_u32_e32 v240, v240, v235
	v_add_u32_e32 v241, v241, v239
	v_lshl_add_u32 v242, v241, 16, v240
	s_nop 1
	v_add_u32_dpp v242, v242, v242 row_shr:1 row_mask:0xf bank_mask:0xf bound_ctrl:1
	s_nop 1
	v_add_u32_dpp v242, v242, v242 row_shr:2 row_mask:0xf bank_mask:0xf bound_ctrl:1
	s_nop 1
	v_add_u32_dpp v242, v242, v242 row_shr:4 row_mask:0xf bank_mask:0xf bound_ctrl:1
	s_nop 1
	v_add_u32_dpp v242, v242, v242 row_shr:8 row_mask:0xf bank_mask:0xf bound_ctrl:1
	s_nop 1
	v_add_u32_dpp v242, v242, v242 row_bcast:15 row_mask:0xa bank_mask:0xf
	s_nop 1
	v_add_u32_dpp v242, v242, v242 row_bcast:31 row_mask:0xc bank_mask:0xf
	s_nop 1
	v_readlane_b32 s20, v242, 63
	s_nop 1
	v_sub_u32_e32 v243, s20, v242
	v_and_b32_e32 v244, 0xffff, v243
	v_lshrrev_b32_e32 v246, 16, v243
	v_cmp_gt_u32_e64 s[58:59], s9, v244
	v_add_u32_e32 v245, v244, v240
	v_cmp_le_u32_e64 s[60:61], s9, v245
	s_and_b64 s[58:59], s[58:59], s[60:61]
	s_ff1_i32_b64 s21, s[58:59]
	s_and_b32 s21, s21, 63
	v_readlane_b32 s22, v244, s21
	v_readlane_b32 s23, v235, s21
	v_readlane_b32 s25, v234, s21
	v_readlane_b32 s26, v233, s21
	v_readlane_b32 s27, v232, s21
	s_add_u32 s28, s22, s23
	s_add_u32 s29, s28, s25
	s_add_u32 s32, s29, s26
	s_mov_b32 s37, 0
	s_mov_b32 s43, s27
	s_mov_b32 s85, s32
	s_cmp_le_u32 s9, s32
	s_cselect_b32 s37, 1, s37
	s_cselect_b32 s43, s26, s43
	s_cselect_b32 s85, s29, s85
	s_cmp_le_u32 s9, s29
	s_cselect_b32 s37, 2, s37
	s_cselect_b32 s43, s25, s43
	s_cselect_b32 s85, s28, s85
	s_cmp_le_u32 s9, s28
	s_cselect_b32 s37, 3, s37
	s_cselect_b32 s43, s23, s43
	s_cselect_b32 s85, s22, s85
	s_lshl_b32 s21, s21, 2
	s_add_i32 s21, s21, s37
	s_lshl_b32 s21, s21, s11
	s_or_b32 s21, s21, s7
	s_sub_i32 s22, s9, s85
	s_cmp_eq_u32 s43, s22
	s_cselect_b32 s23, 1, 0
	s_cmp_lg_u32 s12, 0
	s_cselect_b32 s7, s7, s21
	s_cselect_b32 s9, s9, s22
	s_cselect_b32 s12, 1, s23
	v_cmp_gt_u32_e64 s[58:59], s10, v246
	v_add_u32_e32 v245, v246, v241
	v_cmp_le_u32_e64 s[60:61], s10, v245
	s_and_b64 s[58:59], s[58:59], s[60:61]
	s_ff1_i32_b64 s21, s[58:59]
	s_and_b32 s21, s21, 63
	v_readlane_b32 s22, v246, s21
	v_readlane_b32 s23, v239, s21
	v_readlane_b32 s25, v238, s21
	v_readlane_b32 s26, v237, s21
	v_readlane_b32 s27, v236, s21
	s_add_u32 s28, s22, s23
	s_add_u32 s29, s28, s25
	s_add_u32 s32, s29, s26
	s_mov_b32 s37, 0
	s_mov_b32 s43, s27
	s_mov_b32 s85, s32
	s_cmp_le_u32 s10, s32
	s_cselect_b32 s37, 1, s37
	s_cselect_b32 s43, s26, s43
	s_cselect_b32 s85, s29, s85
	s_cmp_le_u32 s10, s29
	s_cselect_b32 s37, 2, s37
	s_cselect_b32 s43, s25, s43
	s_cselect_b32 s85, s28, s85
	s_cmp_le_u32 s10, s28
	s_cselect_b32 s37, 3, s37
	s_cselect_b32 s43, s23, s43
	s_cselect_b32 s85, s22, s85
	s_lshl_b32 s21, s21, 2
	s_add_i32 s21, s21, s37
	s_lshl_b32 s21, s21, s11
	s_or_b32 s21, s21, s8
	s_sub_i32 s22, s10, s85
	s_cmp_eq_u32 s43, s22
	s_cselect_b32 s23, 1, 0
	s_cmp_lg_u32 s13, 0
	s_cselect_b32 s8, s8, s21
	s_cselect_b32 s10, s10, s22
	s_cselect_b32 s13, 1, s23
	s_sub_i32 s11, s11, 8
	s_cmp_ge_i32 s11, 0
	s_cbranch_scc1 .Lsel_pass_12
